# ring-16 hybrid with adjacency loads sc0 sc1 nt (system scope, non-temporal)
# speedup vs baseline: 1.3339x; 1.3339x over previous
.Lk1_scan:
	s_load_dwordx2 s[4:5], s[0:1], 0x0
	s_load_dwordx4 s[8:11], s[0:1], 0x20
	s_load_dwordx2 s[12:13], s[0:1], 0x30
	v_and_b32_e32 v6, 63, v0
	v_readfirstlane_b32 s3, v0
	v_lshlrev_b32_e32 v1, 4, v6
	v_lshlrev_b32_e32 v2, 2, v6
	v_or_b32_e32 v3, 1, v2
	v_or_b32_e32 v4, 2, v2
	v_or_b32_e32 v5, 3, v2
	s_lshr_b32 s3, s3, 6
	s_sub_u32 s16, s2, 0x60
	s_lshl_b32 s16, s16, 2
	s_add_u32 s16, s16, s3
	s_mul_i32 s17, s16, 0x48000
	s_lshr_b32 s18, s17, 2
	s_lshl_b32 s24, s3, 13
	s_mov_b32 s25, s24
	s_mov_b32 s28, s24
	s_mov_b32 s36, 0
	s_mov_b64 s[62:63], 0
	v_mov_b32_e32 v21, 1
	s_mov_b32 s27, 0
	s_mov_b32 s29, 0x55555556
	s_mov_b32 s31, 0xc0000
	s_waitcnt lgkmcnt(0)
	s_and_b32 s50, s16, 15
	s_mul_i32 s52, s50, 512
	s_add_u32 s52, s52, 28672
	s_lshl_b32 s53, s50, 6
	s_add_u32 s53, s53, 0xe000
	s_add_u32 s54, s10, s53
	s_addc_u32 s55, s11, 0
	s_mul_i32 s59, s16, 14
	s_mul_i32 s57, s59, 0x4000
	s_lshr_b32 s18, s57, 2
	s_add_u32 s6, s4, s57
	s_addc_u32 s7, s5, 0
	v_mov_b32_e32 v27, 0
	global_load_dwordx4 v[28:31], v1, s[6:7] sc0 sc1 nt
	s_add_u32 s6, s6, 0x400
	s_addc_u32 s7, s7, 0
	global_load_dwordx4 v[32:35], v1, s[6:7] sc0 sc1 nt
	s_add_u32 s6, s6, 0x400
	s_addc_u32 s7, s7, 0
	global_load_dwordx4 v[36:39], v1, s[6:7] sc0 sc1 nt
	s_add_u32 s6, s6, 0x400
	s_addc_u32 s7, s7, 0
	global_load_dwordx4 v[40:43], v1, s[6:7] sc0 sc1 nt
	s_add_u32 s6, s6, 0x400
	s_addc_u32 s7, s7, 0
	global_load_dwordx4 v[44:47], v1, s[6:7] sc0 sc1 nt
	s_add_u32 s6, s6, 0x400
	s_addc_u32 s7, s7, 0
	global_load_dwordx4 v[48:51], v1, s[6:7] sc0 sc1 nt
	s_add_u32 s6, s6, 0x400
	s_addc_u32 s7, s7, 0
	global_load_dwordx4 v[52:55], v1, s[6:7] sc0 sc1 nt
	s_add_u32 s6, s6, 0x400
	s_addc_u32 s7, s7, 0
	global_load_dwordx4 v[56:59], v1, s[6:7] sc0 sc1 nt
	s_add_u32 s6, s6, 0x400
	s_addc_u32 s7, s7, 0
	global_load_dwordx4 v[60:63], v1, s[6:7] sc0 sc1 nt
	s_add_u32 s6, s6, 0x400
	s_addc_u32 s7, s7, 0
	global_load_dwordx4 v[64:67], v1, s[6:7] sc0 sc1 nt
	s_add_u32 s6, s6, 0x400
	s_addc_u32 s7, s7, 0
	global_load_dwordx4 v[68:71], v1, s[6:7] sc0 sc1 nt
	s_add_u32 s6, s6, 0x400
	s_addc_u32 s7, s7, 0
	global_load_dwordx4 v[72:75], v1, s[6:7] sc0 sc1 nt
	s_add_u32 s6, s6, 0x400
	s_addc_u32 s7, s7, 0
	global_load_dwordx4 v[76:79], v1, s[6:7] sc0 sc1 nt
	s_add_u32 s6, s6, 0x400
	s_addc_u32 s7, s7, 0
	global_load_dwordx4 v[80:83], v1, s[6:7] sc0 sc1 nt
	s_add_u32 s6, s6, 0x400
	s_addc_u32 s7, s7, 0
	global_load_dwordx4 v[84:87], v1, s[6:7] sc0 sc1 nt
	s_add_u32 s6, s6, 0x400
	s_addc_u32 s7, s7, 0
	global_load_dwordx4 v[88:91], v1, s[6:7] sc0 sc1 nt
	s_add_u32 s6, s6, 0x400
	s_addc_u32 s7, s7, 0
	s_mov_b32 s26, 18
	s_add_u32 s57, s59, 1
	s_mul_i32 s57, s57, 0x4000
	s_lshr_b32 s58, s57, 2
	s_add_u32 s6, s4, s57
	s_addc_u32 s7, s5, 0
	s_mov_b32 s26, 0

.Lk1_contm_7:
	global_load_dwordx4 v[28:31], v1, s[6:7] sc0 sc1 nt
	s_add_u32 s6, s6, 0x400
	s_addc_u32 s7, s7, 0
	global_load_dwordx4 v[32:35], v1, s[6:7] sc0 sc1 nt
	s_add_u32 s6, s6, 0x400
	s_addc_u32 s7, s7, 0
	global_load_dwordx4 v[36:39], v1, s[6:7] sc0 sc1 nt
	s_add_u32 s6, s6, 0x400
	s_addc_u32 s7, s7, 0
	global_load_dwordx4 v[40:43], v1, s[6:7] sc0 sc1 nt
	s_add_u32 s6, s6, 0x400
	s_addc_u32 s7, s7, 0
	global_load_dwordx4 v[44:47], v1, s[6:7] sc0 sc1 nt
	s_add_u32 s6, s6, 0x400
	s_addc_u32 s7, s7, 0
	global_load_dwordx4 v[48:51], v1, s[6:7] sc0 sc1 nt
	s_add_u32 s6, s6, 0x400
	s_addc_u32 s7, s7, 0
	global_load_dwordx4 v[52:55], v1, s[6:7] sc0 sc1 nt
	s_add_u32 s6, s6, 0x400
	s_addc_u32 s7, s7, 0
	global_load_dwordx4 v[56:59], v1, s[6:7] sc0 sc1 nt
	s_add_u32 s6, s6, 0x400
	s_addc_u32 s7, s7, 0
	s_waitcnt vmcnt(15)
	v_or3_b32 v12, v60, v61, v62
	v_or_b32_e32 v12, v12, v63
	v_cmp_ne_u32_e32 vcc, 0, v12
	s_cbranch_vccnz .Lk1_hitm_8

.Lk1_contm_15:
	global_load_dwordx4 v[60:63], v1, s[6:7] sc0 sc1 nt
	s_add_u32 s6, s6, 0x400
	s_addc_u32 s7, s7, 0
	global_load_dwordx4 v[64:67], v1, s[6:7] sc0 sc1 nt
	s_add_u32 s6, s6, 0x400
	s_addc_u32 s7, s7, 0
	global_load_dwordx4 v[68:71], v1, s[6:7] sc0 sc1 nt
	s_add_u32 s6, s6, 0x400
	s_addc_u32 s7, s7, 0
	global_load_dwordx4 v[72:75], v1, s[6:7] sc0 sc1 nt
	s_add_u32 s6, s6, 0x400
	s_addc_u32 s7, s7, 0
	global_load_dwordx4 v[76:79], v1, s[6:7] sc0 sc1 nt
	s_add_u32 s6, s6, 0x400
	s_addc_u32 s7, s7, 0
	global_load_dwordx4 v[80:83], v1, s[6:7] sc0 sc1 nt
	s_add_u32 s6, s6, 0x400
	s_addc_u32 s7, s7, 0
	global_load_dwordx4 v[84:87], v1, s[6:7] sc0 sc1 nt
	s_add_u32 s6, s6, 0x400
	s_addc_u32 s7, s7, 0
	global_load_dwordx4 v[88:91], v1, s[6:7] sc0 sc1 nt
	s_add_u32 s6, s6, 0x400
	s_addc_u32 s7, s7, 0
	s_mov_b32 s18, s58
	s_add_u32 s60, s26, 2
	s_cmp_lt_u32 s60, 14
	s_cbranch_scc0 .Lk1_dynid
	s_add_u32 s57, s59, s60
	s_branch .Lk1_haveid
